# speedup vs baseline: 1.0048x; 1.0025x over previous
_Z12scan2_kernelPKDF16_S0_S0_S0_S0_PKfS2_S2_S2_PDF16_PfS4_:
	s_and_b32 s3, s2, 7
	s_lshr_b32 s2, s2, 3
	s_lshl_b32 s3, s3, 5
	s_or_b32 s2, s2, s3
	s_load_dwordx8 s[4:11], s[0:1], 0x0
	s_load_dwordx8 s[12:19], s[0:1], 0x20
	s_load_dwordx4 s[20:23], s[0:1], 0x40
	s_load_dwordx2 s[24:25], s[0:1], 0x50
	s_and_b32 s26, s2, 3
	s_bfe_u32 s27, s2, 0x50002
	s_lshr_b32 s28, s2, 7
	s_lshl_b32 s29, s26, 3
	v_lshrrev_b32_e32 v1, 6, v0
	v_and_b32_e32 v2, 15, v0
	v_bfe_u32 v3, v0, 4, 2
	v_and_b32_e32 v42, 63, v0
	v_readfirstlane_b32 s40, v1
	v_mov_b32_e32 v43, v0
	v_lshrrev_b32_e32 v14, 4, v43
	v_and_b32_e32 v15, 15, v43
	v_and_b32_e32 v188, 15, v14
	v_xor_b32_e32 v15, v15, v188
	v_lshlrev_b32_e32 v15, 4, v15
	v_lshl_or_b32 v4, v14, 13, v15
	v_lshl_or_b32 v6, v14, 8, v15
	v_lshrrev_b32_e32 v14, 3, v43
	v_and_b32_e32 v15, 7, v43
	v_and_b32_e32 v188, 7, v14
	v_xor_b32_e32 v15, v15, v188
	v_lshlrev_b32_e32 v15, 4, v15
	v_lshl_or_b32 v8, v14, 12, v15
	v_lshlrev_b32_e32 v40, 4, v43
	v_add_u32_e32 v32, 0xc800, v40
	v_add_u32_e32 v43, 0x200, v0
	v_lshrrev_b32_e32 v14, 4, v43
	v_and_b32_e32 v15, 15, v43
	v_and_b32_e32 v188, 15, v14
	v_xor_b32_e32 v15, v15, v188
	v_lshlrev_b32_e32 v15, 4, v15
	v_lshl_or_b32 v5, v14, 13, v15
	v_lshl_or_b32 v7, v14, 8, v15
	v_lshrrev_b32_e32 v14, 3, v43
	v_and_b32_e32 v15, 7, v43
	v_and_b32_e32 v188, 7, v14
	v_xor_b32_e32 v15, v15, v188
	v_lshlrev_b32_e32 v15, 4, v15
	v_lshl_or_b32 v9, v14, 12, v15
	v_lshlrev_b32_e32 v41, 4, v43
	v_add_u32_e32 v33, 0xc800, v41
	s_sub_u32 s45, 11, s40
	s_cmp_lt_u32 s40, 4
	s_cselect_b32 s41, s40, s45
	s_lshr_b32 s42, s41, 1
	s_lshl_b32 s43, s40, 10
	s_lshl_b32 s44, s40, 8
	s_and_b32 s45, s40, 1
	s_lshl_b32 s45, s45, 8
	v_lshl_add_u32 v10, v42, 2, s45
	s_lshl_b32 s45, s41, 4
	v_add_u32_e32 v14, s45, v2
	v_add_u32_e32 v15, 0, v3
	v_xor_b32_e32 v15, v15, v2
	v_lshlrev_b32_e32 v15, 4, v15
	v_lshl_or_b32 v16, v2, 8, v15
	v_add_u32_e32 v20, 0xc800, v16
	v_add_u32_e32 v15, 4, v3
	v_xor_b32_e32 v15, v15, v2
	v_lshlrev_b32_e32 v15, 4, v15
	v_lshl_or_b32 v17, v2, 8, v15
	v_add_u32_e32 v21, 0xc800, v17
	v_add_u32_e32 v15, 8, v3
	v_xor_b32_e32 v15, v15, v2
	v_lshlrev_b32_e32 v15, 4, v15
	v_lshl_or_b32 v18, v2, 8, v15
	v_add_u32_e32 v22, 0xc800, v18
	v_add_u32_e32 v15, 12, v3
	v_xor_b32_e32 v15, v15, v2
	v_lshlrev_b32_e32 v15, 4, v15
	v_lshl_or_b32 v19, v2, 8, v15
	v_add_u32_e32 v23, 0xc800, v19
	v_lshrrev_b32_e32 v188, 1, v3
	v_and_b32_e32 v189, 7, v14
	v_and_b32_e32 v190, 1, v3
	v_lshlrev_b32_e32 v190, 3, v190
	v_lshl_or_b32 v190, v14, 7, v190
	v_add_u32_e32 v15, 0, v188
	v_xor_b32_e32 v15, v15, v189
	v_lshl_add_u32 v24, v15, 4, v190
	v_add_u32_e32 v28, 0xc800, v24
	v_add_u32_e32 v15, 2, v188
	v_xor_b32_e32 v15, v15, v189
	v_lshl_add_u32 v25, v15, 4, v190
	v_add_u32_e32 v29, 0xc800, v25
	v_add_u32_e32 v15, 4, v188
	v_xor_b32_e32 v15, v15, v189
	v_lshl_add_u32 v26, v15, 4, v190
	v_add_u32_e32 v30, 0xc800, v26
	v_add_u32_e32 v15, 6, v188
	v_xor_b32_e32 v15, v15, v189
	v_lshl_add_u32 v27, v15, 4, v190
	v_add_u32_e32 v31, 0xc800, v27
	v_lshlrev_b32_e32 v242, 12, v14
	v_lshl_add_u32 v242, v3, 3, v242
	v_lshlrev_b32_e32 v36, 2, v14
	v_add_u32_e32 v37, 0xc800, v36
	v_lshlrev_b32_e32 v38, 5, v3
	v_add_u32_e32 v39, 0xc800, v38
	s_and_b32 s45, s41, 1
	s_lshl_b32 s45, s45, 4
	v_add_u32_e32 v43, s45, v2
	v_lshlrev_b32_e32 v189, 3, v3
	v_sub_u32_e32 v43, v43, v189
	v_cmp_le_i32_e64 s[52:53], 0, v43
	v_cmp_le_i32_e64 s[54:55], 1, v43
	v_cmp_le_i32_e64 s[56:57], 2, v43
	v_cmp_le_i32_e64 s[58:59], 3, v43
	v_cmp_le_i32_e64 s[60:61], 4, v43
	v_cmp_le_i32_e64 s[62:63], 5, v43
	v_cmp_le_i32_e64 s[64:65], 6, v43
	v_cmp_le_i32_e64 s[66:67], 7, v43
	v_cmp_eq_u32_e32 vcc, 0, v43
	s_nop 1
	v_cndmask_b32_e64 v188, 0, 1.0, vcc
	v_cmp_eq_u32_e32 vcc, 1, v43
	s_nop 1
	v_cndmask_b32_e64 v189, 0, 1.0, vcc
	v_cmp_eq_u32_e32 vcc, 2, v43
	s_nop 1
	v_cndmask_b32_e64 v190, 0, 1.0, vcc
	v_cmp_eq_u32_e32 vcc, 3, v43
	s_nop 1
	v_cndmask_b32_e64 v191, 0, 1.0, vcc
	v_cmp_eq_u32_e32 vcc, 4, v43
	s_nop 1
	v_cndmask_b32_e64 v192, 0, 1.0, vcc
	v_cmp_eq_u32_e32 vcc, 5, v43
	s_nop 1
	v_cndmask_b32_e64 v193, 0, 1.0, vcc
	v_cmp_eq_u32_e32 vcc, 6, v43
	s_nop 1
	v_cndmask_b32_e64 v194, 0, 1.0, vcc
	v_cmp_eq_u32_e32 vcc, 7, v43
	s_nop 1
	v_cndmask_b32_e64 v195, 0, 1.0, vcc
	v_cvt_pk_f16_f32 v92, v188, v189
	v_cvt_pk_f16_f32 v93, v190, v191
	v_cvt_pk_f16_f32 v94, v192, v193
	v_cvt_pk_f16_f32 v95, v194, v195
	v_mov_b32_e32 v250, 0
	v_mov_b32_e32 v251, 0
	s_waitcnt lgkmcnt(0)
	s_lshl_b32 s45, s28, 12
	s_lshl_b32 s48, s27, 7
	s_add_u32 s45, s45, s48
	s_lshl_b32 s48, s45, 9
	s_add_u32 s48, s4, s48
	s_addc_u32 s49, s5, 0
	v_lshlrev_b32_e32 v188, 9, v14
	v_lshl_add_u32 v188, v3, 4, v188
	global_load_dwordx4 v[44:47], v188, s[48:49] offset:256
	global_load_dwordx4 v[48:51], v188, s[48:49] offset:320
	global_load_dwordx4 v[52:55], v188, s[48:49] offset:384
	global_load_dwordx4 v[56:59], v188, s[48:49] offset:448
	s_lshl_b32 s48, s28, 5
	s_add_u32 s48, s48, s27
	s_lshl_b32 s48, s48, 15
	s_add_u32 s48, s10, s48
	s_addc_u32 s49, s11, 0
	v_lshlrev_b32_e32 v188, 8, v14
	v_lshl_add_u32 v188, v3, 4, v188
	global_load_dwordx4 v[144:147], v188, s[48:49] offset:0
	global_load_dwordx4 v[148:151], v188, s[48:49] offset:64
	global_load_dwordx4 v[152:155], v188, s[48:49] offset:128
	global_load_dwordx4 v[156:159], v188, s[48:49] offset:192
	v_and_b32_e32 v188, 7, v42
	v_add_u32_e32 v188, s29, v188
	v_lshlrev_b32_e32 v188, 2, v188
	global_load_dword v11, v188, s[20:21]
	global_load_dword v12, v188, s[18:19]
	s_mul_i32 s48, s28, 0x900
	s_lshl_b32 s49, s29, 6
	s_add_u32 s48, s48, s49
	s_lshl_b32 s48, s48, 13
	s_lshl_b32 s49, s27, 8
	s_add_u32 s48, s48, s49
	s_add_u32 s30, s6, s48
	s_addc_u32 s31, s7, 0
	s_lshl_b32 s48, s28, 5
	s_add_u32 s48, s48, s27
	s_lshl_b32 s48, s48, 5
	s_add_u32 s48, s48, s29
	s_lshl_b32 s48, s48, 14
	s_add_u32 s32, s12, s48
	s_addc_u32 s33, s13, 0
	s_lshl_b32 s48, s45, 12
	s_lshl_b32 s49, s29, 7
	s_add_u32 s48, s48, s49
	s_add_u32 s34, s8, s48
	s_addc_u32 s35, s9, 0
	s_add_u32 s38, s22, s48
	s_addc_u32 s39, s23, 0
	s_lshl_b32 s48, s28, 5
	s_add_u32 s48, s48, s29
	s_lshl_b32 s48, s48, 14
	s_lshl_b32 s49, s27, 9
	s_add_u32 s48, s48, s49
	s_lshr_b32 s49, s40, 1
	s_cmp_eq_u32 s49, 1
	s_cselect_b32 s50, s14, s16
	s_cselect_b32 s51, s15, s17
	s_add_u32 s36, s50, s48
	s_addc_u32 s37, s51, 0
	s_lshl_b32 s48, s45, 2
	s_add_u32 s24, s24, s48
	s_addc_u32 s25, s25, 0
	v_lshlrev_b32_e32 v15, 2, v14
	s_mov_b32 s51, 0xbfb8aa3b
	s_mov_b32 s50, 0x41800000
	s_add_u32 m0, s43, 0x0
	s_nop 0
	global_load_lds_dwordx4 v4, s[30:31]
	s_add_u32 m0, s43, 0x4000
	s_nop 0
	global_load_lds_dwordx4 v6, s[32:33]
	s_add_u32 m0, s43, 0x8000
	s_nop 0
	global_load_lds_dwordx4 v8, s[34:35]
	s_add_u32 m0, s43, 0x2000
	s_nop 0
	global_load_lds_dwordx4 v5, s[30:31]
	s_add_u32 m0, s43, 0x6000
	s_nop 0
	global_load_lds_dwordx4 v7, s[32:33]
	s_add_u32 m0, s43, 0xa000
	s_nop 0
	global_load_lds_dwordx4 v9, s[34:35]
	s_add_u32 m0, s44, 0xc000
	s_nop 0
	global_load_lds_dword v10, s[36:37]
	s_add_u32 s30, s30, 0x80000
	s_addc_u32 s31, s31, 0
	s_add_u32 s32, s32, 0x4000
	s_addc_u32 s33, s33, 0
	s_add_u32 s34, s34, 0x80
	s_addc_u32 s35, s35, 0
	s_add_u32 s36, s36, 0x4000
	s_addc_u32 s37, s37, 0
	global_load_dword v243, v10, s[36:37]
	global_load_dword v243, v10, s[36:37]
	global_load_dword v243, v10, s[36:37]
	global_load_dword v243, v10, s[36:37]
	s_waitcnt vmcnt(16)
	v_cvt_f32_f16_e32 v60, v144
	v_cvt_f32_f16_sdwa v61, v144 dst_sel:DWORD dst_unused:UNUSED_PAD src0_sel:WORD_1
	v_cvt_f32_f16_e32 v62, v145
	v_cvt_f32_f16_sdwa v63, v145 dst_sel:DWORD dst_unused:UNUSED_PAD src0_sel:WORD_1
	v_cvt_f32_f16_e32 v64, v146
	v_cvt_f32_f16_sdwa v65, v146 dst_sel:DWORD dst_unused:UNUSED_PAD src0_sel:WORD_1
	v_cvt_f32_f16_e32 v66, v147
	v_cvt_f32_f16_sdwa v67, v147 dst_sel:DWORD dst_unused:UNUSED_PAD src0_sel:WORD_1
	s_waitcnt vmcnt(15)
	v_cvt_f32_f16_e32 v68, v148
	v_cvt_f32_f16_sdwa v69, v148 dst_sel:DWORD dst_unused:UNUSED_PAD src0_sel:WORD_1
	v_cvt_f32_f16_e32 v70, v149
	v_cvt_f32_f16_sdwa v71, v149 dst_sel:DWORD dst_unused:UNUSED_PAD src0_sel:WORD_1
	v_cvt_f32_f16_e32 v72, v150
	v_cvt_f32_f16_sdwa v73, v150 dst_sel:DWORD dst_unused:UNUSED_PAD src0_sel:WORD_1
	v_cvt_f32_f16_e32 v74, v151
	v_cvt_f32_f16_sdwa v75, v151 dst_sel:DWORD dst_unused:UNUSED_PAD src0_sel:WORD_1
	s_waitcnt vmcnt(14)
	v_cvt_f32_f16_e32 v76, v152
	v_cvt_f32_f16_sdwa v77, v152 dst_sel:DWORD dst_unused:UNUSED_PAD src0_sel:WORD_1
	v_cvt_f32_f16_e32 v78, v153
	v_cvt_f32_f16_sdwa v79, v153 dst_sel:DWORD dst_unused:UNUSED_PAD src0_sel:WORD_1
	v_cvt_f32_f16_e32 v80, v154
	v_cvt_f32_f16_sdwa v81, v154 dst_sel:DWORD dst_unused:UNUSED_PAD src0_sel:WORD_1
	v_cvt_f32_f16_e32 v82, v155
	v_cvt_f32_f16_sdwa v83, v155 dst_sel:DWORD dst_unused:UNUSED_PAD src0_sel:WORD_1
	s_waitcnt vmcnt(13)
	v_cvt_f32_f16_e32 v84, v156
	v_cvt_f32_f16_sdwa v85, v156 dst_sel:DWORD dst_unused:UNUSED_PAD src0_sel:WORD_1
	v_cvt_f32_f16_e32 v86, v157
	v_cvt_f32_f16_sdwa v87, v157 dst_sel:DWORD dst_unused:UNUSED_PAD src0_sel:WORD_1
	v_cvt_f32_f16_e32 v88, v158
	v_cvt_f32_f16_sdwa v89, v158 dst_sel:DWORD dst_unused:UNUSED_PAD src0_sel:WORD_1
	v_cvt_f32_f16_e32 v90, v159
	v_cvt_f32_f16_sdwa v91, v159 dst_sel:DWORD dst_unused:UNUSED_PAD src0_sel:WORD_1
	s_waitcnt vmcnt(11)
	s_waitcnt vmcnt(12)
	v_mul_f32_e32 v11, 0x41800000, v11
	v_mov_b32_e32 v212, v16
	v_mov_b32_e32 v216, v24
	v_mov_b32_e32 v213, v17
	v_mov_b32_e32 v217, v25
	v_mov_b32_e32 v214, v18
	v_mov_b32_e32 v218, v26
	v_mov_b32_e32 v215, v19
	v_mov_b32_e32 v219, v27
	v_mov_b32_e32 v220, v36
	v_mov_b32_e32 v221, v38
	s_mov_b32 s70, 0xc800
	s_mov_b32 s71, 0xc800
	s_mov_b32 s48, 0
.Lmy_s2_heads1:
	s_waitcnt vmcnt(4)
	s_add_u32 s49, s48, 0
	s_waitcnt lgkmcnt(0)
	s_barrier
	ds_read_b128 v[144:147], v212 offset:16384
	ds_read_b128 v[148:151], v212 offset:20480
	ds_read_b128 v[152:155], v212 offset:24576
	ds_read_b128 v[156:159], v212 offset:28672
	ds_read_b32 v189, v220 offset:49152
	s_cmp_lt_u32 s49, 7
	s_cbranch_scc0 .Lmy_s2_nodma3
	s_add_u32 s72, s43, s71
	s_add_u32 s73, s44, s71
	s_add_u32 m0, s72, 0x0
	s_nop 0
	global_load_lds_dwordx4 v4, s[30:31]
	s_add_u32 m0, s72, 0x4000
	s_nop 0
	global_load_lds_dwordx4 v6, s[32:33]
	s_add_u32 m0, s72, 0x8000
	s_nop 0
	global_load_lds_dwordx4 v8, s[34:35]
	s_add_u32 m0, s72, 0x2000
	s_nop 0
	global_load_lds_dwordx4 v5, s[30:31]
	s_add_u32 m0, s72, 0x6000
	s_nop 0
	global_load_lds_dwordx4 v7, s[32:33]
	s_add_u32 m0, s72, 0xa000
	s_nop 0
	global_load_lds_dwordx4 v9, s[34:35]
	s_add_u32 m0, s73, 0xc000
	s_nop 0
	global_load_lds_dword v10, s[36:37]
	s_add_u32 s30, s30, 0x80000
	s_addc_u32 s31, s31, 0
	s_add_u32 s32, s32, 0x4000
	s_addc_u32 s33, s33, 0
	s_add_u32 s34, s34, 0x80
	s_addc_u32 s35, s35, 0
	s_add_u32 s36, s36, 0x4000
	s_addc_u32 s37, s37, 0
.Lmy_s2_nodma3:
	ds_read_b128 v[160:163], v213 offset:16384
	ds_read_b128 v[164:167], v213 offset:20480
	ds_read_b128 v[168:171], v213 offset:24576
	ds_read_b128 v[172:175], v213 offset:28672
	s_waitcnt lgkmcnt(4)
	v_mfma_f32_16x16x32_f16 v[96:99], v[144:147], v[44:47], 0
	v_mfma_f32_16x16x32_f16 v[100:103], v[148:151], v[44:47], 0
	v_mfma_f32_16x16x32_f16 v[104:107], v[152:155], v[44:47], 0
	v_mfma_f32_16x16x32_f16 v[108:111], v[156:159], v[44:47], 0
	ds_read_b128 v[144:147], v214 offset:16384
	ds_read_b128 v[148:151], v214 offset:20480
	ds_read_b128 v[152:155], v214 offset:24576
	ds_read_b128 v[156:159], v214 offset:28672
	s_waitcnt lgkmcnt(4)
	v_mfma_f32_16x16x32_f16 v[96:99], v[160:163], v[48:51], v[96:99]
	v_mfma_f32_16x16x32_f16 v[100:103], v[164:167], v[48:51], v[100:103]
	v_mfma_f32_16x16x32_f16 v[104:107], v[168:171], v[48:51], v[104:107]
	v_mfma_f32_16x16x32_f16 v[108:111], v[172:175], v[48:51], v[108:111]
	ds_read_b128 v[160:163], v215 offset:16384
	ds_read_b128 v[164:167], v215 offset:20480
	ds_read_b128 v[168:171], v215 offset:24576
	ds_read_b128 v[172:175], v215 offset:28672
	s_waitcnt lgkmcnt(4)
	v_mfma_f32_16x16x32_f16 v[96:99], v[144:147], v[52:55], v[96:99]
	v_mfma_f32_16x16x32_f16 v[100:103], v[148:151], v[52:55], v[100:103]
	v_mfma_f32_16x16x32_f16 v[104:107], v[152:155], v[52:55], v[104:107]
	v_mfma_f32_16x16x32_f16 v[108:111], v[156:159], v[52:55], v[108:111]
	ds_read_b128 v[176:179], v221 offset:49664
	ds_read_b128 v[180:183], v221 offset:49680
	ds_read_b32 v188, v221 offset:49152
	ds_read_b128 v[144:147], v212 offset:0
	ds_read_b128 v[148:151], v212 offset:4096
	ds_read_b128 v[152:155], v212 offset:8192
	ds_read_b128 v[156:159], v212 offset:12288
	s_waitcnt lgkmcnt(7)
	v_mfma_f32_16x16x32_f16 v[96:99], v[160:163], v[56:59], v[96:99]
	v_mfma_f32_16x16x32_f16 v[100:103], v[164:167], v[56:59], v[100:103]
	v_mfma_f32_16x16x32_f16 v[104:107], v[168:171], v[56:59], v[104:107]
	v_mfma_f32_16x16x32_f16 v[108:111], v[172:175], v[56:59], v[108:111]
	v_mul_f32_e32 v189, 0x3fb8aa3b, v189
	s_cmp_lt_u32 s42, 0
	s_cbranch_scc1 .Lmy_s2_kend4
	s_cmp_eq_u32 s42, 0
	s_cbranch_scc1 .Lmy_s2_diag5
	ds_read_b128 v[224:227], v221 offset:49792
	ds_read_b128 v[228:231], v221 offset:49808
	ds_read_b32 v232, v221 offset:49280
	ds_read_b128 v[160:163], v213 offset:0
	ds_read_b128 v[164:167], v213 offset:4096
	ds_read_b128 v[168:171], v213 offset:8192
	ds_read_b128 v[172:175], v213 offset:12288
	s_waitcnt lgkmcnt(7)
	v_fma_f32 v188, v188, s51, v189
	v_exp_f32_e32 v188, v188
	s_nop 0
	v_pk_mul_f32 v[176:177], v[176:177], v[188:189] op_sel_hi:[1,0]
	v_pk_mul_f32 v[178:179], v[178:179], v[188:189] op_sel_hi:[1,0]
	v_pk_mul_f32 v[180:181], v[180:181], v[188:189] op_sel_hi:[1,0]
	v_pk_mul_f32 v[182:183], v[182:183], v[188:189] op_sel_hi:[1,0]
	v_pk_mul_f32 v[176:177], v[60:61], v[176:177]
	v_pk_mul_f32 v[178:179], v[62:63], v[178:179]
	v_pk_mul_f32 v[180:181], v[64:65], v[180:181]
	v_pk_mul_f32 v[182:183], v[66:67], v[182:183]
	v_cvt_pk_f16_f32 v184, v176, v177
	v_cvt_pk_f16_f32 v185, v178, v179
	v_cvt_pk_f16_f32 v186, v180, v181
	v_cvt_pk_f16_f32 v187, v182, v183
	s_nop 1
	v_mfma_f32_16x16x32_f16 v[112:115], v[144:147], v[184:187], 0
	v_mfma_f32_16x16x32_f16 v[116:119], v[148:151], v[184:187], 0
	v_mfma_f32_16x16x32_f16 v[120:123], v[152:155], v[184:187], 0
	v_mfma_f32_16x16x32_f16 v[124:127], v[156:159], v[184:187], 0
	s_branch .Lmy_s2_knext6

.Lmy_s2_knext12:
.Lmy_s2_kend4:
	v_readlane_b32 s46, v11, s49
	v_readlane_b32 s47, v12, s49
	v_exp_f32_e32 v190, v189
	s_waitcnt lgkmcnt(0)
	s_nop 7
	v_cvt_f32_f16_e32 v198, v234
	v_cvt_f32_f16_sdwa v199, v234 dst_sel:DWORD dst_unused:UNUSED_PAD src0_sel:WORD_1
	v_cvt_f32_f16_e32 v200, v235
	v_cvt_f32_f16_sdwa v201, v235 dst_sel:DWORD dst_unused:UNUSED_PAD src0_sel:WORD_1
	v_pk_fma_f32 v[192:193], v[190:191], v[96:97], v[112:113] op_sel_hi:[0,1,1]
	v_pk_fma_f32 v[194:195], v[190:191], v[98:99], v[114:115] op_sel_hi:[0,1,1]
	v_pk_mul_f32 v[192:193], v[192:193], s[46:47] op_sel:[0,1] op_sel_hi:[1,1]
	v_pk_mul_f32 v[194:195], v[194:195], s[46:47] op_sel:[0,1] op_sel_hi:[1,1]
	v_pk_fma_f32 v[192:193], s[46:47], v[128:129], v[192:193] op_sel_hi:[0,1,1]
	v_pk_fma_f32 v[194:195], s[46:47], v[130:131], v[194:195] op_sel_hi:[0,1,1]
	v_pk_mul_f32 v[192:193], v[192:193], v[198:199]
	v_pk_mul_f32 v[194:195], v[194:195], v[200:201]
	v_pk_fma_f32 v[250:251], v[192:193], v[192:193], v[250:251]
	v_pk_fma_f32 v[250:251], v[194:195], v[194:195], v[250:251]
	v_cvt_pk_f16_f32 v196, v192, v193
	v_cvt_pk_f16_f32 v197, v194, v195
	global_store_dwordx2 v242, v[196:197], s[38:39]
	v_cvt_f32_f16_e32 v198, v236
	v_cvt_f32_f16_sdwa v199, v236 dst_sel:DWORD dst_unused:UNUSED_PAD src0_sel:WORD_1
	v_cvt_f32_f16_e32 v200, v237
	v_cvt_f32_f16_sdwa v201, v237 dst_sel:DWORD dst_unused:UNUSED_PAD src0_sel:WORD_1
	v_pk_fma_f32 v[192:193], v[190:191], v[100:101], v[116:117] op_sel_hi:[0,1,1]
	v_pk_fma_f32 v[194:195], v[190:191], v[102:103], v[118:119] op_sel_hi:[0,1,1]
	v_pk_mul_f32 v[192:193], v[192:193], s[46:47] op_sel:[0,1] op_sel_hi:[1,1]
	v_pk_mul_f32 v[194:195], v[194:195], s[46:47] op_sel:[0,1] op_sel_hi:[1,1]
	v_pk_fma_f32 v[192:193], s[46:47], v[132:133], v[192:193] op_sel_hi:[0,1,1]
	v_pk_fma_f32 v[194:195], s[46:47], v[134:135], v[194:195] op_sel_hi:[0,1,1]
	v_pk_mul_f32 v[192:193], v[192:193], v[198:199]
	v_pk_mul_f32 v[194:195], v[194:195], v[200:201]
	v_pk_fma_f32 v[250:251], v[192:193], v[192:193], v[250:251]
	v_pk_fma_f32 v[250:251], v[194:195], v[194:195], v[250:251]
	v_cvt_pk_f16_f32 v196, v192, v193
	v_cvt_pk_f16_f32 v197, v194, v195
	global_store_dwordx2 v242, v[196:197], s[38:39] offset:32
	v_cvt_f32_f16_e32 v198, v238
	v_cvt_f32_f16_sdwa v199, v238 dst_sel:DWORD dst_unused:UNUSED_PAD src0_sel:WORD_1
	v_cvt_f32_f16_e32 v200, v239
	v_cvt_f32_f16_sdwa v201, v239 dst_sel:DWORD dst_unused:UNUSED_PAD src0_sel:WORD_1
	v_pk_fma_f32 v[192:193], v[190:191], v[104:105], v[120:121] op_sel_hi:[0,1,1]
	v_pk_fma_f32 v[194:195], v[190:191], v[106:107], v[122:123] op_sel_hi:[0,1,1]
	v_pk_mul_f32 v[192:193], v[192:193], s[46:47] op_sel:[0,1] op_sel_hi:[1,1]
	v_pk_mul_f32 v[194:195], v[194:195], s[46:47] op_sel:[0,1] op_sel_hi:[1,1]
	v_pk_fma_f32 v[192:193], s[46:47], v[136:137], v[192:193] op_sel_hi:[0,1,1]
	v_pk_fma_f32 v[194:195], s[46:47], v[138:139], v[194:195] op_sel_hi:[0,1,1]
	v_pk_mul_f32 v[192:193], v[192:193], v[198:199]
	v_pk_mul_f32 v[194:195], v[194:195], v[200:201]
	v_pk_fma_f32 v[250:251], v[192:193], v[192:193], v[250:251]
	v_pk_fma_f32 v[250:251], v[194:195], v[194:195], v[250:251]
	v_cvt_pk_f16_f32 v196, v192, v193
	v_cvt_pk_f16_f32 v197, v194, v195
	global_store_dwordx2 v242, v[196:197], s[38:39] offset:64
	v_cvt_f32_f16_e32 v198, v240
	v_cvt_f32_f16_sdwa v199, v240 dst_sel:DWORD dst_unused:UNUSED_PAD src0_sel:WORD_1
	v_cvt_f32_f16_e32 v200, v241
	v_cvt_f32_f16_sdwa v201, v241 dst_sel:DWORD dst_unused:UNUSED_PAD src0_sel:WORD_1
	v_pk_fma_f32 v[192:193], v[190:191], v[108:109], v[124:125] op_sel_hi:[0,1,1]
	v_pk_fma_f32 v[194:195], v[190:191], v[110:111], v[126:127] op_sel_hi:[0,1,1]
	v_pk_mul_f32 v[192:193], v[192:193], s[46:47] op_sel:[0,1] op_sel_hi:[1,1]
	v_pk_mul_f32 v[194:195], v[194:195], s[46:47] op_sel:[0,1] op_sel_hi:[1,1]
	v_pk_fma_f32 v[192:193], s[46:47], v[140:141], v[192:193] op_sel_hi:[0,1,1]
	v_pk_fma_f32 v[194:195], s[46:47], v[142:143], v[194:195] op_sel_hi:[0,1,1]
	v_pk_mul_f32 v[192:193], v[192:193], v[198:199]
	v_pk_mul_f32 v[194:195], v[194:195], v[200:201]
	v_pk_fma_f32 v[250:251], v[192:193], v[192:193], v[250:251]
	v_pk_fma_f32 v[250:251], v[194:195], v[194:195], v[250:251]
	v_cvt_pk_f16_f32 v196, v192, v193
	v_cvt_pk_f16_f32 v197, v194, v195
	global_store_dwordx2 v242, v[196:197], s[38:39] offset:96
	s_add_u32 s38, s38, 0x80
	s_addc_u32 s39, s39, 0
	v_add_u32_e32 v212, s70, v212
	v_add_u32_e32 v213, s70, v213
	v_add_u32_e32 v214, s70, v214
	v_add_u32_e32 v215, s70, v215
	v_add_u32_e32 v216, s70, v216
	v_add_u32_e32 v217, s70, v217
	v_add_u32_e32 v218, s70, v218
	v_add_u32_e32 v219, s70, v219
	v_add_u32_e32 v220, s70, v220
	v_add_u32_e32 v221, s70, v221
	s_sub_u32 s70, 0, s70
	s_sub_u32 s71, 0xc800, s71
	s_add_u32 s48, s48, 1
	s_cmp_lt_u32 s48, 8
	s_cbranch_scc1 .Lmy_s2_heads1
	v_add_f32_e32 v13, v250, v251
	v_mul_f32_e32 v13, 0x3b800000, v13
	v_mbcnt_lo_u32_b32 v188, -1, 0
	v_mbcnt_hi_u32_b32 v188, -1, v188
	v_xor_b32_e32 v189, 16, v188
	v_lshlrev_b32_e32 v189, 2, v189
	ds_bpermute_b32 v190, v189, v13
	s_waitcnt lgkmcnt(0)
	v_add_f32_e32 v13, v13, v190
	v_xor_b32_e32 v189, 32, v188
	v_lshlrev_b32_e32 v189, 2, v189
	ds_bpermute_b32 v190, v189, v13
	s_waitcnt lgkmcnt(0)
	v_add_f32_e32 v13, v13, v190
	v_cmp_gt_u32_e32 vcc, 16, v188
	s_and_saveexec_b64 s[48:49], vcc
	s_cbranch_execz .Lmy_s2_noat13
	global_atomic_add_f32 v15, v13, s[24:25]
